# p0 weight-conversion f32 loads marked nt (read-once stream), on top of NSA + MoE-order changes
# baseline (speedup 1.0000x reference)
; __device__ __forceinline__ void witem_load(const WItem& w, f32x4 (&v)[16]) {
;     if (!w.valid) return;
; #pragma unroll
;     for (int i = 0; i < 16; ++i) v[i] = *(const f32x4*)(w.src + (size_t)i * w.N);
; }
; __device__ __forceinline__ void p0_weights(const Args& a, LAS unsigned char* lds) {
;     ...
;     { f32x4 v[16], vn[16];
;       WItem cur = decode(gw); witem_load(cur, v);
.LBB0_45:
	s_lshl_b64 s[10:11], s[10:11], 2
	v_lshl_add_u64 v[6:7], v[66:67], 0, s[10:11]
	v_lshl_add_u64 v[14:15], v[6:7], 0, s[10:11]
	global_load_dwordx4 v[2:5], v[66:67], off nt
	s_nop 0
	global_load_dwordx4 v[6:9], v[6:7], off nt
	s_nop 0
	global_load_dwordx4 v[10:13], v[14:15], off nt
	v_lshl_add_u64 v[14:15], v[14:15], 0, s[10:11]
	v_lshl_add_u64 v[22:23], v[14:15], 0, s[10:11]
	global_load_dwordx4 v[14:17], v[14:15], off nt
	s_nop 0
	global_load_dwordx4 v[18:21], v[22:23], off nt
	v_lshl_add_u64 v[22:23], v[22:23], 0, s[10:11]
	v_lshl_add_u64 v[30:31], v[22:23], 0, s[10:11]
	global_load_dwordx4 v[22:25], v[22:23], off nt
	s_nop 0
	global_load_dwordx4 v[26:29], v[30:31], off nt
	v_lshl_add_u64 v[30:31], v[30:31], 0, s[10:11]
	v_lshl_add_u64 v[38:39], v[30:31], 0, s[10:11]
	global_load_dwordx4 v[30:33], v[30:31], off nt
	s_nop 0
	global_load_dwordx4 v[34:37], v[38:39], off nt
	v_lshl_add_u64 v[38:39], v[38:39], 0, s[10:11]
	v_lshl_add_u64 v[46:47], v[38:39], 0, s[10:11]
	v_lshl_add_u64 v[50:51], v[46:47], 0, s[10:11]
	v_lshl_add_u64 v[54:55], v[50:51], 0, s[10:11]
	v_lshl_add_u64 v[58:59], v[54:55], 0, s[10:11]
	v_lshl_add_u64 v[62:63], v[58:59], 0, s[10:11]
	global_load_dwordx4 v[38:41], v[38:39], off nt
	s_nop 0
	global_load_dwordx4 v[42:45], v[46:47], off nt
	s_nop 0
	global_load_dwordx4 v[46:49], v[50:51], off nt
	s_nop 0
	global_load_dwordx4 v[50:53], v[54:55], off nt
	s_nop 0
	global_load_dwordx4 v[54:57], v[58:59], off nt
	s_nop 0
	global_load_dwordx4 v[58:61], v[62:63], off nt
	v_lshl_add_u64 v[62:63], v[62:63], 0, s[10:11]
	global_load_dwordx4 v[62:65], v[62:63], off nt

; __device__ __forceinline__ void witem_load(const WItem& w, f32x4 (&v)[16]) {
;     if (!w.valid) return;
; #pragma unroll
;     for (int i = 0; i < 16; ++i) v[i] = *(const f32x4*)(w.src + (size_t)i * w.N);
; }
; __device__ __forceinline__ void p0_weights(const Args& a, LAS unsigned char* lds) {
;     ...
;     { f32x4 v[16], vn[16];
;       WItem cur = decode(gw); witem_load(cur, v);
; #pragma unroll 1
;       for (int it = gw; it < NIT; it += NGW) {
;           const WItem nxt = decode(it + NGW); witem_load(nxt, vn);
;           __builtin_amdgcn_sched_barrier(0);
;           witem_store(cur, v);
;           __builtin_amdgcn_sched_barrier(0);
; #pragma unroll
;           for (int i = 0; i < 16; ++i) v[i] = vn[i];
;           cur = nxt; } }
.LBB0_75:
	s_lshl_b64 s[24:25], s[24:25], 2
	v_lshl_add_u64 v[6:7], v[134:135], 0, s[24:25]
	v_lshl_add_u64 v[14:15], v[6:7], 0, s[24:25]
	global_load_dwordx4 v[2:5], v[134:135], off nt
	s_nop 0
	global_load_dwordx4 v[6:9], v[6:7], off nt
	s_nop 0
	global_load_dwordx4 v[10:13], v[14:15], off nt
	v_lshl_add_u64 v[14:15], v[14:15], 0, s[24:25]
	v_lshl_add_u64 v[22:23], v[14:15], 0, s[24:25]
	global_load_dwordx4 v[14:17], v[14:15], off nt
	s_nop 0
	global_load_dwordx4 v[18:21], v[22:23], off nt
	v_lshl_add_u64 v[22:23], v[22:23], 0, s[24:25]
	v_lshl_add_u64 v[30:31], v[22:23], 0, s[24:25]
	global_load_dwordx4 v[22:25], v[22:23], off nt
	s_nop 0
	global_load_dwordx4 v[26:29], v[30:31], off nt
	v_lshl_add_u64 v[30:31], v[30:31], 0, s[24:25]
	v_lshl_add_u64 v[38:39], v[30:31], 0, s[24:25]
	global_load_dwordx4 v[30:33], v[30:31], off nt
	s_nop 0
	global_load_dwordx4 v[34:37], v[38:39], off nt
	v_lshl_add_u64 v[38:39], v[38:39], 0, s[24:25]
	v_lshl_add_u64 v[46:47], v[38:39], 0, s[24:25]
	v_lshl_add_u64 v[50:51], v[46:47], 0, s[24:25]
	v_lshl_add_u64 v[54:55], v[50:51], 0, s[24:25]
	v_lshl_add_u64 v[58:59], v[54:55], 0, s[24:25]
	v_lshl_add_u64 v[62:63], v[58:59], 0, s[24:25]
	global_load_dwordx4 v[38:41], v[38:39], off nt
	s_nop 0
	global_load_dwordx4 v[42:45], v[46:47], off nt
	s_nop 0
	global_load_dwordx4 v[46:49], v[50:51], off nt
	s_nop 0
	global_load_dwordx4 v[50:53], v[54:55], off nt
	s_nop 0
	global_load_dwordx4 v[54:57], v[58:59], off nt
	s_nop 0
	global_load_dwordx4 v[58:61], v[62:63], off nt
	v_lshl_add_u64 v[62:63], v[62:63], 0, s[24:25]
	global_load_dwordx4 v[62:65], v[62:63], off nt
